# baseline (speedup 1.0000x reference)
.LBB3_8:
	s_mul_i32 s33, s33, 0x401100
	s_waitcnt lgkmcnt(0)
	s_add_u32 s0, s6, s33
	s_addc_u32 s1, s7, 0
	v_lshlrev_b32_e32 v8, 4, v96
	v_mov_b32_e32 v9, 0
	s_and_b32 s2, s2, -8
	v_lshl_add_u64 v[10:11], s[0:1], 0, v[8:9]
	s_movk_i32 s0, 0x110
	v_mad_u32_u24 v0, v108, s0, v8
	v_lshl_or_b32 v4, s2, 6, v108
	s_waitcnt vmcnt(0)
	s_barrier
	ds_read_b128 v[16:19], v0
	v_lshrrev_b32_e32 v4, 4, v97
	v_mad_u32_u24 v4, v4, s0, v8
	ds_read_b128 v[20:23], v4
	v_lshrrev_b32_e32 v4, 4, v102
	v_mad_u32_u24 v4, v4, s0, v8
	ds_read_b128 v[24:27], v4
	v_lshrrev_b32_e32 v4, 4, v103
	v_mad_u32_u24 v4, v4, s0, v8
	ds_read_b128 v[28:31], v4
	v_lshrrev_b32_e32 v4, 4, v104
	v_mad_u32_u24 v4, v4, s0, v8
	ds_read_b128 v[32:35], v4
	v_lshrrev_b32_e32 v4, 4, v105
	v_mad_u32_u24 v4, v4, s0, v8
	ds_read_b128 v[36:39], v4
	v_lshrrev_b32_e32 v4, 4, v106
	v_mad_u32_u24 v4, v4, s0, v8
	ds_read_b128 v[40:43], v4
	v_lshrrev_b32_e32 v4, 4, v107
	v_mad_u32_u24 v4, v4, s0, v8
	ds_read_b128 v[44:47], v4
	v_lshl_or_b32 v4, s2, 6, v108
	v_or_b32_e32 v4, s3, v4
	v_ashrrev_i32_e32 v5, 31, v4
	v_lshlrev_b64 v[4:5], 8, v[4:5]
	v_lshl_add_u64 v[48:49], v[10:11], 0, v[4:5]
	v_lshrrev_b32_e32 v4, 9, v97
	v_or_b32_e32 v4, s2, v4
	v_lshlrev_b32_e32 v4, 6, v4
	v_or3_b32 v4, v4, v108, s3
	v_ashrrev_i32_e32 v5, 31, v4
	v_lshlrev_b64 v[4:5], 8, v[4:5]
	v_lshl_add_u64 v[50:51], v[10:11], 0, v[4:5]
	v_lshrrev_b32_e32 v4, 9, v102
	v_or_b32_e32 v4, s2, v4
	v_lshlrev_b32_e32 v4, 6, v4
	v_or3_b32 v4, v4, v108, s3
	v_ashrrev_i32_e32 v5, 31, v4
	v_lshlrev_b64 v[4:5], 8, v[4:5]
	v_lshl_add_u64 v[52:53], v[10:11], 0, v[4:5]
	v_lshrrev_b32_e32 v4, 9, v103
	v_or_b32_e32 v4, s2, v4
	v_lshlrev_b32_e32 v4, 6, v4
	v_or3_b32 v4, v4, v108, s3
	v_ashrrev_i32_e32 v5, 31, v4
	v_lshlrev_b64 v[4:5], 8, v[4:5]
	v_lshl_add_u64 v[54:55], v[10:11], 0, v[4:5]
	v_lshrrev_b32_e32 v4, 9, v104
	v_or_b32_e32 v4, s2, v4
	v_lshlrev_b32_e32 v4, 6, v4
	v_or3_b32 v4, v4, v108, s3
	v_ashrrev_i32_e32 v5, 31, v4
	v_lshlrev_b64 v[4:5], 8, v[4:5]
	v_lshl_add_u64 v[56:57], v[10:11], 0, v[4:5]
	v_lshrrev_b32_e32 v4, 9, v105
	v_or_b32_e32 v4, s2, v4
	v_lshlrev_b32_e32 v4, 6, v4
	v_or3_b32 v4, v4, v108, s3
	v_ashrrev_i32_e32 v5, 31, v4
	v_lshlrev_b64 v[4:5], 8, v[4:5]
	v_lshl_add_u64 v[58:59], v[10:11], 0, v[4:5]
	v_lshrrev_b32_e32 v4, 9, v106
	v_or_b32_e32 v4, s2, v4
	v_lshlrev_b32_e32 v4, 6, v4
	v_or3_b32 v4, v4, v108, s3
	v_ashrrev_i32_e32 v5, 31, v4
	v_lshlrev_b64 v[4:5], 8, v[4:5]
	v_lshl_add_u64 v[60:61], v[10:11], 0, v[4:5]
	v_lshrrev_b32_e32 v4, 9, v107
	v_or_b32_e32 v4, s2, v4
	v_lshlrev_b32_e32 v4, 6, v4
	v_or3_b32 v4, v4, v108, s3
	v_ashrrev_i32_e32 v5, 31, v4
	v_lshlrev_b64 v[4:5], 8, v[4:5]
	v_lshl_add_u64 v[62:63], v[10:11], 0, v[4:5]
	s_waitcnt lgkmcnt(7)
	global_store_dwordx4 v[48:49], v[16:19], off nt
	s_waitcnt lgkmcnt(6)
	global_store_dwordx4 v[50:51], v[20:23], off nt
	s_waitcnt lgkmcnt(5)
	global_store_dwordx4 v[52:53], v[24:27], off nt
	s_waitcnt lgkmcnt(4)
	global_store_dwordx4 v[54:55], v[28:31], off nt
	s_waitcnt lgkmcnt(3)
	global_store_dwordx4 v[56:57], v[32:35], off nt
	s_waitcnt lgkmcnt(2)
	global_store_dwordx4 v[58:59], v[36:39], off nt
	s_waitcnt lgkmcnt(1)
	global_store_dwordx4 v[60:61], v[40:43], off nt
	s_waitcnt lgkmcnt(0)
	global_store_dwordx4 v[62:63], v[44:47], off nt
	s_endpgm
	.p2align	8
